# speedup vs baseline: 1.0123x; 1.0123x over previous
.LBB0_12:
	s_ashr_i32 s13, s12, 31
	s_lshl_b64 s[0:1], s[12:13], 14
	v_lshl_or_b32 v68, v0, 3, s0
	v_mov_b32_e32 v69, s1
	s_waitcnt lgkmcnt(0)
	v_lshl_add_u64 v[0:1], v[68:69], 2, s[8:9]
	global_load_dwordx4 v[16:19], v[0:1], off sc1 nt
	global_load_dwordx4 v[20:23], v[0:1], off offset:16 sc1 nt
	s_mov_b64 s[8:9], 0x2000
	v_lshl_add_u64 v[2:3], v[0:1], 0, s[8:9]
	global_load_dwordx4 v[24:27], v[2:3], off sc1 nt
	global_load_dwordx4 v[28:31], v[2:3], off offset:16 sc1 nt
	s_mov_b64 s[2:3], 0x4000
	v_lshl_add_u64 v[2:3], v[0:1], 0, s[2:3]
	global_load_dwordx4 v[32:35], v[2:3], off sc1 nt
	global_load_dwordx4 v[36:39], v[2:3], off offset:16 sc1 nt
	s_mov_b64 s[0:1], 0x6000
	v_lshl_add_u64 v[2:3], v[0:1], 0, s[0:1]
	global_load_dwordx4 v[40:43], v[2:3], off sc1 nt
	global_load_dwordx4 v[44:47], v[2:3], off offset:16 sc1 nt
	s_mov_b64 s[10:11], 0x8000
	v_lshl_add_u64 v[2:3], v[0:1], 0, s[10:11]
	global_load_dwordx4 v[48:51], v[2:3], off sc1 nt
	global_load_dwordx4 v[52:55], v[2:3], off offset:16 sc1 nt
	s_mov_b64 s[10:11], 0xa000
	v_lshl_add_u64 v[2:3], v[0:1], 0, s[10:11]
	s_mov_b64 s[10:11], 0xc000
	global_load_dwordx4 v[56:59], v[2:3], off sc1 nt
	global_load_dwordx4 v[60:63], v[2:3], off offset:16 sc1 nt
	v_lshl_add_u64 v[4:5], v[0:1], 0, s[10:11]
	s_mov_b64 s[10:11], 0xe000
	global_load_dwordx4 v[12:15], v[4:5], off sc1 nt
	global_load_dwordx4 v[8:11], v[4:5], off offset:16 sc1 nt
	v_lshl_add_u64 v[64:65], v[0:1], 0, s[10:11]
	global_load_dwordx4 v[4:7], v[64:65], off sc1 nt
	global_load_dwordx4 v[0:3], v[64:65], off offset:16 sc1 nt
	s_nop 0
	s_waitcnt vmcnt(15)
	s_nop 0
	s_waitcnt vmcnt(14)
	v_mov_b32_e32 v64, v21
	v_mov_b32_e32 v65, v22
	v_pk_mul_f32 v[64:65], s[4:5], v[64:65] op_sel_hi:[0,1]
	v_cvt_pk_f16_f32 v66, v64, v65
	v_lshrrev_b32_e32 v67, 16, v66
	v_fma_mixhi_f16 v67, s4, v23, 0
	v_mov_b32_e32 v22, v17
	v_mov_b32_e32 v23, v18
	v_pk_mov_b32 v[20:21], v[18:19], v[20:21] op_sel:[1,0]
	v_fma_mixlo_f16 v18, s4, v16, 0
	v_pk_mul_f32 v[16:17], s[4:5], v[22:23] op_sel_hi:[0,1]
	v_cvt_pk_f16_f32 v19, v16, v17
	v_pk_mul_f32 v[16:17], s[4:5], v[20:21] op_sel_hi:[0,1]
	v_cvt_pk_f16_f32 v16, v16, v17
	v_alignbit_b32 v65, v16, v19, 16
	v_alignbit_b32 v66, v66, v16, 16
	s_waitcnt vmcnt(12)
	v_mov_b32_e32 v16, v29
	v_mov_b32_e32 v17, v30
	v_pk_mul_f32 v[16:17], s[4:5], v[16:17] op_sel_hi:[0,1]
	v_pack_b32_f16 v64, v18, v19
	v_cvt_pk_f16_f32 v18, v16, v17
	v_pk_mov_b32 v[16:17], v[26:27], v[28:29] op_sel:[1,0]
	v_mov_b32_e32 v22, v25
	v_mov_b32_e32 v23, v26
	v_pk_mul_f32 v[22:23], s[4:5], v[22:23] op_sel_hi:[0,1]
	v_pk_mul_f32 v[16:17], s[4:5], v[16:17] op_sel_hi:[0,1]
	v_fma_mixlo_f16 v24, s4, v24, 0
	v_cvt_pk_f16_f32 v22, v22, v23
	v_cvt_pk_f16_f32 v23, v16, v17
	v_lshl_add_u64 v[20:21], v[68:69], 1, s[6:7]
	global_store_dwordx4 v[20:21], v[64:67], off sc1
	s_nop 1
	v_lshrrev_b32_e32 v19, 16, v18
	v_pack_b32_f16 v16, v24, v22
	v_alignbit_b32 v17, v23, v22, 16
	s_mov_b64 s[6:7], 0x1000
	v_fma_mixhi_f16 v19, s4, v31, 0
	v_alignbit_b32 v18, v18, v23, 16
	v_lshl_add_u64 v[22:23], v[20:21], 0, s[6:7]
	global_store_dwordx4 v[22:23], v[16:19], off sc1
	s_nop 1
	s_waitcnt vmcnt(13)
	v_mov_b32_e32 v16, v33
	v_mov_b32_e32 v17, v34
	v_pk_mul_f32 v[16:17], s[4:5], v[16:17] op_sel_hi:[0,1]
	s_waitcnt vmcnt(12)
	v_pk_mov_b32 v[18:19], v[34:35], v[36:37] op_sel:[1,0]
	v_fma_mixlo_f16 v22, s4, v32, 0
	v_cvt_pk_f16_f32 v17, v16, v17
	v_pk_mul_f32 v[18:19], s[4:5], v[18:19] op_sel_hi:[0,1]
	v_pack_b32_f16 v16, v22, v17
	v_cvt_pk_f16_f32 v22, v18, v19
	v_mov_b32_e32 v18, v37
	v_mov_b32_e32 v19, v38
	v_pk_mul_f32 v[18:19], s[4:5], v[18:19] op_sel_hi:[0,1]
	v_cvt_pk_f16_f32 v19, v18, v19
	v_alignbit_b32 v17, v22, v17, 16
	v_alignbit_b32 v18, v19, v22, 16
	v_lshrrev_b32_e32 v19, 16, v19
	v_fma_mixhi_f16 v19, s4, v39, 0
	v_lshl_add_u64 v[22:23], v[20:21], 0, s[8:9]
	global_store_dwordx4 v[22:23], v[16:19], off sc1
	s_nop 1
	s_waitcnt vmcnt(12)
	v_mov_b32_e32 v16, v41
	v_mov_b32_e32 v17, v42
	v_pk_mul_f32 v[16:17], s[4:5], v[16:17] op_sel_hi:[0,1]
	v_fma_mixlo_f16 v18, s4, v40, 0
	v_cvt_pk_f16_f32 v17, v16, v17
	v_pack_b32_f16 v16, v18, v17
	s_waitcnt vmcnt(11)
	v_pk_mov_b32 v[18:19], v[42:43], v[44:45] op_sel:[1,0]
	s_mov_b64 s[6:7], 0x3000
	v_pk_mul_f32 v[18:19], s[4:5], v[18:19] op_sel_hi:[0,1]
	v_cvt_pk_f16_f32 v22, v18, v19
	v_mov_b32_e32 v18, v45
	v_mov_b32_e32 v19, v46
	v_pk_mul_f32 v[18:19], s[4:5], v[18:19] op_sel_hi:[0,1]
	v_cvt_pk_f16_f32 v19, v18, v19
	v_alignbit_b32 v17, v22, v17, 16
	v_alignbit_b32 v18, v19, v22, 16
	v_lshrrev_b32_e32 v19, 16, v19
	v_fma_mixhi_f16 v19, s4, v47, 0
	v_lshl_add_u64 v[22:23], v[20:21], 0, s[6:7]
	global_store_dwordx4 v[22:23], v[16:19], off sc1
	s_nop 1
	s_waitcnt vmcnt(11)
	v_mov_b32_e32 v16, v49
	v_mov_b32_e32 v17, v50
	v_pk_mul_f32 v[16:17], s[4:5], v[16:17] op_sel_hi:[0,1]
	v_fma_mixlo_f16 v18, s4, v48, 0
	v_cvt_pk_f16_f32 v17, v16, v17
	v_pack_b32_f16 v16, v18, v17
	s_waitcnt vmcnt(10)
	v_pk_mov_b32 v[18:19], v[50:51], v[52:53] op_sel:[1,0]
	s_nop 0
	v_pk_mul_f32 v[18:19], s[4:5], v[18:19] op_sel_hi:[0,1]
	v_cvt_pk_f16_f32 v22, v18, v19
	v_mov_b32_e32 v18, v53
	v_mov_b32_e32 v19, v54
	v_pk_mul_f32 v[18:19], s[4:5], v[18:19] op_sel_hi:[0,1]
	v_cvt_pk_f16_f32 v19, v18, v19
	v_alignbit_b32 v17, v22, v17, 16
	v_alignbit_b32 v18, v19, v22, 16
	v_lshrrev_b32_e32 v19, 16, v19
	v_fma_mixhi_f16 v19, s4, v55, 0
	v_lshl_add_u64 v[22:23], v[20:21], 0, s[2:3]
	global_store_dwordx4 v[22:23], v[16:19], off sc1
	s_nop 1
	s_waitcnt vmcnt(10)
	v_mov_b32_e32 v16, v57
	v_mov_b32_e32 v17, v58
	v_pk_mul_f32 v[16:17], s[4:5], v[16:17] op_sel_hi:[0,1]
	v_fma_mixlo_f16 v18, s4, v56, 0
	v_cvt_pk_f16_f32 v17, v16, v17
	v_pack_b32_f16 v16, v18, v17
	s_waitcnt vmcnt(9)
	v_pk_mov_b32 v[18:19], v[58:59], v[60:61] op_sel:[1,0]
	s_mov_b64 s[2:3], 0x5000
	v_pk_mul_f32 v[18:19], s[4:5], v[18:19] op_sel_hi:[0,1]
	v_cvt_pk_f16_f32 v22, v18, v19
	v_mov_b32_e32 v18, v61
	v_mov_b32_e32 v19, v62
	v_pk_mul_f32 v[18:19], s[4:5], v[18:19] op_sel_hi:[0,1]
	v_cvt_pk_f16_f32 v19, v18, v19
	v_alignbit_b32 v18, v19, v22, 16
	v_lshrrev_b32_e32 v19, 16, v19
	v_alignbit_b32 v17, v22, v17, 16
	v_fma_mixhi_f16 v19, s4, v63, 0
	v_lshl_add_u64 v[22:23], v[20:21], 0, s[2:3]
	global_store_dwordx4 v[22:23], v[16:19], off sc1
	s_nop 1
	s_waitcnt vmcnt(9)
	v_fma_mixlo_f16 v16, s4, v12, 0
	v_mov_b32_e32 v12, v13
	v_mov_b32_e32 v13, v14
	s_waitcnt vmcnt(8)
	v_pk_mov_b32 v[14:15], v[14:15], v[8:9] op_sel:[1,0]
	v_mov_b32_e32 v8, v9
	v_mov_b32_e32 v9, v10
	v_pk_mul_f32 v[12:13], s[4:5], v[12:13] op_sel_hi:[0,1]
	v_pk_mul_f32 v[14:15], s[4:5], v[14:15] op_sel_hi:[0,1]
	v_pk_mul_f32 v[8:9], s[4:5], v[8:9] op_sel_hi:[0,1]
	v_cvt_pk_f16_f32 v13, v12, v13
	v_cvt_pk_f16_f32 v14, v14, v15
	v_cvt_pk_f16_f32 v8, v8, v9
	v_pack_b32_f16 v12, v16, v13
	v_alignbit_b32 v13, v14, v13, 16
	v_alignbit_b32 v14, v8, v14, 16
	v_lshrrev_b32_e32 v15, 16, v8
	v_lshl_add_u64 v[8:9], v[20:21], 0, s[0:1]
	v_fma_mixhi_f16 v15, s4, v11, 0
	global_store_dwordx4 v[8:9], v[12:15], off sc1
	s_nop 1
	s_waitcnt vmcnt(8)
	v_fma_mixlo_f16 v8, s4, v4, 0
	v_mov_b32_e32 v4, v5
	v_mov_b32_e32 v5, v6
	s_waitcnt vmcnt(7)
	v_pk_mov_b32 v[6:7], v[6:7], v[0:1] op_sel:[1,0]
	v_mov_b32_e32 v0, v1
	v_mov_b32_e32 v1, v2
	v_pk_mul_f32 v[0:1], s[4:5], v[0:1] op_sel_hi:[0,1]
	v_pk_mul_f32 v[4:5], s[4:5], v[4:5] op_sel_hi:[0,1]
	v_pk_mul_f32 v[6:7], s[4:5], v[6:7] op_sel_hi:[0,1]
	v_cvt_pk_f16_f32 v0, v0, v1
	v_cvt_pk_f16_f32 v5, v4, v5
	v_cvt_pk_f16_f32 v6, v6, v7
	v_lshrrev_b32_e32 v7, 16, v0
	s_mov_b64 s[0:1], 0x7000
	v_pack_b32_f16 v4, v8, v5
	v_alignbit_b32 v5, v6, v5, 16
	v_alignbit_b32 v6, v0, v6, 16
	v_fma_mixhi_f16 v7, s4, v3, 0
	v_lshl_add_u64 v[0:1], v[20:21], 0, s[0:1]
	global_store_dwordx4 v[0:1], v[4:7], off sc1
	s_nop 1
	s_endpgm
